# h1 (RMSNorm+adaLN) rows dealt only to workgroups 128..255 (two 4-row chunks per wave); workgroups 0..127, which still run the SSM table preparation, skip it
# baseline (speedup 1.0000x reference)
.LBB0_368:
.LBB0_369:
	s_cmp_lt_i32 s92, 2
	s_cselect_b64 s[2:3], -1, 0
	s_and_b64 s[0:1], s[2:3], s[0:1]
	s_andn2_b64 vcc, exec, s[0:1]
	s_lshr_b32 s80, s78, 6
	s_cbranch_vccnz .LBB0_374
	s_sub_i32 s0, s96, 0x80
	s_cmp_lt_i32 s0, 0
	s_cbranch_scc1 .LBB0_373
	s_lshl_b32 s0, s0, 3
	s_add_i32 s11, s0, s80
	v_mbcnt_lo_u32_b32 v1, -1, 0
	v_mbcnt_hi_u32_b32 v2, -1, v1
	v_and_b32_e32 v1, 64, v2
	v_add_u32_e32 v3, 64, v1
	v_xor_b32_e32 v1, 32, v2
	v_cmp_lt_i32_e32 vcc, v1, v3
	v_xor_b32_e32 v4, 16, v2
	v_mov_b32_e32 v5, 0
	v_cndmask_b32_e32 v1, v2, v1, vcc
	v_cmp_lt_i32_e32 vcc, v4, v3
	s_add_u32 s22, s70, 0x8000
	s_mov_b64 s[0:1], 0x38000
	v_cndmask_b32_e32 v4, v2, v4, vcc
	v_lshlrev_b32_e32 v159, 2, v4
	v_xor_b32_e32 v4, 8, v2
	v_cmp_lt_i32_e32 vcc, v4, v3
	s_addc_u32 s23, s71, 0
	v_lshlrev_b32_e32 v1, 2, v1
	v_cndmask_b32_e32 v4, v2, v4, vcc
	v_lshlrev_b32_e32 v171, 2, v4
	v_xor_b32_e32 v4, 4, v2
	v_cmp_lt_i32_e32 vcc, v4, v3
	s_movk_i32 s24, 0x1000
	s_mov_b32 s10, 0x3a000000
	v_cndmask_b32_e32 v4, v2, v4, vcc
	v_lshlrev_b32_e32 v244, 2, v4
	v_xor_b32_e32 v4, 2, v2
	v_cmp_lt_i32_e32 vcc, v4, v3
	s_mov_b32 s25, 0x800000
	s_nop 0
	v_cndmask_b32_e32 v4, v2, v4, vcc
	v_lshlrev_b32_e32 v245, 2, v4
	v_xor_b32_e32 v4, 1, v2
	v_cmp_lt_i32_e32 vcc, v4, v3
	s_nop 1
	v_cndmask_b32_e32 v2, v2, v4, vcc
	v_lshlrev_b32_e32 v246, 2, v2
	v_lshlrev_b32_e32 v2, 2, v170
	v_lshlrev_b32_e32 v4, 4, v170
	s_waitcnt vmcnt(6)
	v_or_b32_e32 v12, 0x400, v2
	v_lshl_add_u64 v[160:161], s[12:13], 0, v[4:5]
	v_lshl_add_u64 v[162:163], s[20:21], 0, v[4:5]
	v_lshlrev_b32_e32 v4, 2, v12
	s_waitcnt vmcnt(5)
	v_or_b32_e32 v14, 0x500, v2
	v_lshl_add_u64 v[164:165], s[20:21], 0, v[4:5]
	v_lshlrev_b32_e32 v4, 2, v14
	v_or_b32_e32 v16, 0x600, v2
	v_lshl_add_u64 v[166:167], s[20:21], 0, v[4:5]
	v_lshlrev_b32_e32 v4, 2, v16
	s_waitcnt vmcnt(4)
	v_or_b32_e32 v18, 0x700, v2
	v_lshl_add_u64 v[168:169], s[20:21], 0, v[4:5]
	v_lshlrev_b32_e32 v4, 2, v18
	v_lshl_add_u64 v[172:173], s[20:21], 0, v[4:5]
	v_lshlrev_b32_e32 v4, 3, v170
	v_lshl_add_u64 v[4:5], s[70:71], 0, v[4:5]
	v_lshl_add_u64 v[174:175], v[4:5], 0, s[0:1]
	s_sub_i32 s0, s96, 0x80
	s_lshl_b32 s0, s0, 5
	s_lshl_b32 s1, s80, 2
	v_or_b32_e32 v6, 0x100, v2
	v_or_b32_e32 v8, 0x200, v2
	v_or_b32_e32 v10, 0x300, v2
	s_add_i32 s8, s0, s1
	s_mov_b32 s0, 0x358637bd
	s_lshl_b32 s20, s72, 2
	s_lshl_b32 s21, s72, 4
	v_lshlrev_b32_e32 v247, 2, v2
	v_lshlrev_b32_e32 v248, 2, v6
	v_lshlrev_b32_e32 v249, 2, v8
	v_lshlrev_b32_e32 v250, 2, v10
	v_lshlrev_b32_e32 v251, 2, v12
	v_lshlrev_b32_e32 v252, 2, v14
	v_lshlrev_b32_e32 v253, 2, v16
	v_lshlrev_b32_e32 v254, 2, v18
	v_mov_b64_e32 v[176:177], s[0:1]
